# scan pass 1 chunk loop: next-chunk log-decay loads land in free registers, their conversions and the vmcnt wait move from the middle of the MFMA part down to the first use (counted wait leaves the out
# baseline (speedup 1.0000x reference)
.LBB0_355:
	v_lshlrev_b32_e32 v136, 16, v86
	v_cndmask_b32_e64 v86, v108, v107, s[14:15]
	v_cndmask_b32_e64 v58, v86, v58, s[12:13]
	v_cndmask_b32_e64 v139, v58, 0, s[0:1]
	v_sub_f32_e32 v58, v59, v139
	v_lshlrev_b32_e32 v109, 16, v50
	v_lshlrev_b32_e32 v112, 16, v51
	v_and_b32_e32 v51, 0xffff0000, v105
	v_lshlrev_b32_e32 v50, 16, v105
	v_lshlrev_b32_e32 v105, 16, v87
	v_sub_f32_e32 v87, v58, v115
	v_sub_f32_e32 v53, 1.0, v124
	v_sub_f32_e32 v56, 1.0, v121
	v_lshlrev_b32_e32 v121, 16, v60
	v_lshlrev_b32_e32 v124, 16, v61
	v_and_b32_e32 v61, 0xffff0000, v126
	v_lshlrev_b32_e32 v60, 16, v126
	v_lshlrev_b32_e32 v126, 16, v88
	v_exp_f32_e32 v88, v87
	v_sub_f32_e32 v87, v58, v116
	v_and_b32_e32 v65, 0xffff0000, v127
	v_lshlrev_b32_e32 v64, 16, v127
	v_lshlrev_b32_e32 v127, 16, v89
	v_exp_f32_e32 v89, v87
	v_sub_f32_e32 v87, v58, v113
	v_sub_f32_e32 v52, 1.0, v123
	v_sub_f32_e32 v62, 1.0, v119
	v_sub_f32_e32 v123, 1.0, v118
	v_lshlrev_b32_e32 v118, 16, v48
	v_lshlrev_b32_e32 v119, 16, v49
	v_and_b32_e32 v49, 0xffff0000, v100
	v_lshlrev_b32_e32 v48, 16, v100
	v_lshlrev_b32_e32 v100, 16, v92
	v_exp_f32_e32 v92, v87
	v_sub_f32_e32 v87, v58, v114
	v_lshlrev_b32_e32 v138, 16, v93
	v_exp_f32_e32 v93, v87
	v_sub_f32_e32 v133, 1.0, v37
	v_sub_f32_e32 v132, 1.0, v36
	v_sub_f32_e32 v57, 1.0, v122
	v_sub_f32_e32 v122, 1.0, v117
	v_pk_mul_f32 v[88:89], v[132:133], v[88:89]
	v_sub_f32_e32 v63, 1.0, v120
	v_lshlrev_b32_e32 v117, 16, v54
	v_lshlrev_b32_e32 v120, 16, v55
	v_and_b32_e32 v55, 0xffff0000, v125
	v_lshlrev_b32_e32 v54, 16, v125
	v_lshlrev_b32_e32 v125, 16, v90
	v_cvt_pk_bf16_f32 v90, v88, v89
	v_pk_mul_f32 v[88:89], v[122:123], v[92:93]
	v_lshlrev_b32_e32 v137, 16, v91
	v_cvt_pk_bf16_f32 v91, v88, v89
	v_sub_f32_e32 v89, v58, v110
	v_exp_f32_e32 v92, v89
	v_sub_f32_e32 v89, v58, v111
	v_exp_f32_e32 v93, v89
	v_sub_f32_e32 v89, v58, v103
	v_and_b32_e32 v37, 0xffff0000, v106
	v_lshlrev_b32_e32 v36, 16, v106
	v_exp_f32_e32 v106, v89
	v_sub_f32_e32 v89, v58, v104
	v_exp_f32_e32 v107, v89
	v_pk_mul_f32 v[92:93], v[62:63], v[92:93]
	v_cvt_pk_bf16_f32 v86, v109, v112
	v_cvt_pk_bf16_f32 v92, v92, v93
	v_pk_mul_f32 v[106:107], v[56:57], v[106:107]
	v_cvt_pk_bf16_f32 v88, v119, v120
	v_cvt_pk_bf16_f32 v93, v106, v107
	v_sub_f32_e32 v107, v58, v101
	v_exp_f32_e32 v108, v107
	v_sub_f32_e32 v107, v58, v102
	v_exp_f32_e32 v109, v107
	v_sub_f32_e32 v107, v58, v98
	v_exp_f32_e32 v120, v107
	v_sub_f32_e32 v107, v58, v99
	v_cvt_pk_bf16_f32 v89, v121, v124
	v_exp_f32_e32 v121, v107
	v_sub_f32_e32 v39, 1.0, v39
	v_sub_f32_e32 v38, 1.0, v38
	v_pk_mul_f32 v[108:109], v[52:53], v[108:109]
	v_cvt_pk_bf16_f32 v87, v117, v118
	v_cvt_pk_bf16_f32 v118, v108, v109
	v_pk_mul_f32 v[108:109], v[38:39], v[120:121]
	v_cvt_pk_bf16_f32 v107, v125, v136
	v_cvt_pk_bf16_f32 v119, v108, v109
	v_cvt_pk_bf16_f32 v108, v105, v137
	v_sub_f32_e32 v105, v58, v96
	v_exp_f32_e32 v120, v105
	v_sub_f32_e32 v105, v58, v97
	v_exp_f32_e32 v121, v105
	v_sub_f32_e32 v105, v58, v94
	v_sub_f32_e32 v58, v58, v95
	v_exp_f32_e32 v125, v58
	v_add_f32_e32 v58, v115, v139
	v_max_f32_e32 v58, 0xc2e60000, v58
	v_cvt_pk_bf16_f32 v106, v126, v127
	v_cvt_pk_bf16_f32 v109, v100, v138
	ds_write_b128 v79, v[86:89]
	ds_write_b128 v79, v[106:109] offset:16
	v_exp_f32_e32 v86, v58
	v_add_f32_e32 v58, v116, v139
	v_max_f32_e32 v58, 0xc2e60000, v58
	v_exp_f32_e32 v87, v58
	s_lshl_b32 s77, s75, 6
	s_add_i32 s76, s77, s58
	s_add_i32 s80, s76, s60
	v_exp_f32_e32 v124, v105
	s_sub_i32 s81, 0x1fff, s80
	v_rcp_f32_e32 v88, v86
	v_rcp_f32_e32 v89, v87
	v_exp_f32_e32 v58, v69
	s_and_b64 s[78:79], s[10:11], exec
	s_cselect_b32 s78, s80, s81
	v_sub_f32_e32 v33, 1.0, v33
	v_sub_f32_e32 v32, 1.0, v32
	v_sub_f32_e32 v35, 1.0, v35
	v_sub_f32_e32 v34, 1.0, v34
	v_and_b32_e32 v135, 0xffff0000, v129
	v_lshlrev_b32_e32 v134, 16, v129
	s_add_i32 s78, s78, s59
	v_pk_mul_f32 v[120:121], v[34:35], v[120:121]
	v_pk_mul_f32 v[124:125], v[32:33], v[124:125]
	v_pk_mul_f32 v[86:87], v[86:87], v[134:135]
	s_add_i32 s80, s78, s64
	s_ashr_i32 s79, s78, 31
	v_cvt_pk_bf16_f32 v120, v120, v121
	v_cvt_pk_bf16_f32 v121, v124, v125
	ds_write_b128 v80, v[90:93]
	ds_write_b128 v80, v[118:121] offset:16
	v_pk_mul_f32 v[88:89], v[132:133], v[88:89]
	v_cvt_pk_bf16_f32 v91, v86, v87
	v_pk_mul_f32 v[86:87], v[58:59], v[86:87] op_sel_hi:[0,1]
	s_lshl_b64 s[78:79], s[78:79], 11
	s_ashr_i32 s81, s80, 31
	v_cvt_pk_bf16_f32 v90, v88, v89
	v_cvt_pk_bf16_f32 v88, v86, v87
	v_lshl_add_u64 v[86:87], v[44:45], 0, s[78:79]
	s_lshl_b64 s[78:79], s[80:81], 11
	global_store_short v[86:87], v88, off
	v_lshl_add_u64 v[86:87], v[44:45], 0, s[78:79]
	global_store_short_d16_hi v[86:87], v88, off
	v_add_f32_e32 v86, v113, v139
	v_add_f32_e32 v87, v114, v139
	v_max_f32_e32 v86, 0xc2e60000, v86
	v_max_f32_e32 v87, 0xc2e60000, v87
	v_exp_f32_e32 v86, v86
	v_exp_f32_e32 v87, v87
	s_add_i32 s80, s76, s67
	s_sub_i32 s81, 0x1fff, s80
	v_rcp_f32_e32 v88, v86
	v_rcp_f32_e32 v89, v87
	s_and_b64 s[78:79], s[10:11], exec
	s_cselect_b32 s78, s80, s81
	v_and_b32_e32 v129, 0xffff0000, v128
	v_lshlrev_b32_e32 v128, 16, v128
	s_add_i32 s78, s78, s59
	v_add_u32_e32 v92, s66, v72
	v_pk_mul_f32 v[86:87], v[86:87], v[128:129]
	s_add_i32 s80, s78, s64
	s_ashr_i32 s79, s78, 31
	ds_write_b16 v92, v91 offset:4096
	ds_write_b16_d16_hi v92, v91 offset:4368
	ds_write_b16 v92, v90 offset:38912
	ds_write_b16_d16_hi v92, v90 offset:39184
	v_pk_mul_f32 v[88:89], v[122:123], v[88:89]
	v_cvt_pk_bf16_f32 v91, v86, v87
	v_pk_mul_f32 v[86:87], v[58:59], v[86:87] op_sel_hi:[0,1]
	s_lshl_b64 s[78:79], s[78:79], 11
	s_ashr_i32 s81, s80, 31
	v_cvt_pk_bf16_f32 v90, v88, v89
	v_cvt_pk_bf16_f32 v88, v86, v87
	v_lshl_add_u64 v[86:87], v[44:45], 0, s[78:79]
	s_lshl_b64 s[78:79], s[80:81], 11
	global_store_short v[86:87], v88, off
	v_lshl_add_u64 v[86:87], v[44:45], 0, s[78:79]
	global_store_short_d16_hi v[86:87], v88, off
	v_add_f32_e32 v86, v110, v139
	v_add_f32_e32 v87, v111, v139
	v_max_f32_e32 v86, 0xc2e60000, v86
	v_max_f32_e32 v87, 0xc2e60000, v87
	v_exp_f32_e32 v86, v86
	v_exp_f32_e32 v87, v87
	s_add_i32 s80, s76, s69
	s_sub_i32 s81, 0x1fff, s80
	v_rcp_f32_e32 v88, v86
	v_rcp_f32_e32 v89, v87
	s_and_b64 s[78:79], s[10:11], exec
	s_cselect_b32 s78, s80, s81
	s_add_i32 s78, s78, s59
	v_pk_mul_f32 v[62:63], v[62:63], v[88:89]
	s_add_i32 s80, s78, s64
	v_cvt_pk_bf16_f32 v88, v62, v63
	v_pk_mul_f32 v[62:63], v[86:87], v[64:65]
	v_add_f32_e32 v64, v103, v139
	v_add_f32_e32 v65, v104, v139
	v_max_f32_e32 v64, 0xc2e60000, v64
	v_max_f32_e32 v65, 0xc2e60000, v65
	s_ashr_i32 s79, s78, 31
	v_exp_f32_e32 v64, v64
	v_exp_f32_e32 v65, v65
	v_cvt_pk_bf16_f32 v86, v62, v63
	v_pk_mul_f32 v[62:63], v[58:59], v[62:63] op_sel_hi:[0,1]
	s_lshl_b64 s[78:79], s[78:79], 11
	s_ashr_i32 s81, s80, 31
	v_add_u32_e32 v92, s68, v72
	v_cvt_pk_bf16_f32 v87, v62, v63
	v_lshl_add_u64 v[62:63], v[44:45], 0, s[78:79]
	s_lshl_b64 s[78:79], s[80:81], 11
	ds_write_b16 v92, v91 offset:4096
	ds_write_b16_d16_hi v92, v91 offset:4368
	ds_write_b16 v92, v90 offset:38912
	ds_write_b16_d16_hi v92, v90 offset:39184
	global_store_short v[62:63], v87, off
	v_lshl_add_u64 v[62:63], v[44:45], 0, s[78:79]
	global_store_short_d16_hi v[62:63], v87, off
	v_rcp_f32_e32 v62, v64
	v_rcp_f32_e32 v63, v65
	s_add_i32 s80, s76, s70
	s_sub_i32 s81, 0x1fff, s80
	s_and_b64 s[78:79], s[10:11], exec
	v_pk_mul_f32 v[56:57], v[56:57], v[62:63]
	s_cselect_b32 s78, s80, s81
	v_cvt_pk_bf16_f32 v62, v56, v57
	v_pk_mul_f32 v[56:57], v[64:65], v[60:61]
	v_add_f32_e32 v60, v101, v139
	v_add_f32_e32 v61, v102, v139
	s_add_i32 s78, s78, s59
	v_max_f32_e32 v60, 0xc2e60000, v60
	v_max_f32_e32 v61, 0xc2e60000, v61
	s_add_i32 s80, s78, s64
	s_ashr_i32 s79, s78, 31
	v_exp_f32_e32 v60, v60
	v_exp_f32_e32 v61, v61
	v_cvt_pk_bf16_f32 v63, v56, v57
	v_pk_mul_f32 v[56:57], v[58:59], v[56:57] op_sel_hi:[0,1]
	s_lshl_b64 s[78:79], s[78:79], 11
	s_ashr_i32 s81, s80, 31
	v_cvt_pk_bf16_f32 v64, v56, v57
	v_lshl_add_u64 v[56:57], v[44:45], 0, s[78:79]
	s_lshl_b64 s[78:79], s[80:81], 11
	ds_write_b16 v92, v86 offset:4640
	ds_write_b16_d16_hi v92, v86 offset:4912
	ds_write_b16 v92, v88 offset:39456
	ds_write_b16_d16_hi v92, v88 offset:39728
	global_store_short v[56:57], v64, off
	v_lshl_add_u64 v[56:57], v[44:45], 0, s[78:79]
	global_store_short_d16_hi v[56:57], v64, off
	v_rcp_f32_e32 v56, v60
	v_rcp_f32_e32 v57, v61
	s_add_i32 s80, s76, s71
	s_sub_i32 s81, 0x1fff, s80
	s_and_b64 s[78:79], s[10:11], exec
	v_pk_mul_f32 v[52:53], v[52:53], v[56:57]
	s_cselect_b32 s78, s80, s81
	v_cvt_pk_bf16_f32 v56, v52, v53
	v_pk_mul_f32 v[52:53], v[60:61], v[54:55]
	v_add_f32_e32 v54, v98, v139
	v_add_f32_e32 v55, v99, v139
	s_add_i32 s78, s78, s59
	v_max_f32_e32 v54, 0xc2e60000, v54
	v_max_f32_e32 v55, 0xc2e60000, v55
	s_add_i32 s80, s78, s64
	s_ashr_i32 s79, s78, 31
	v_exp_f32_e32 v54, v54
	v_exp_f32_e32 v55, v55
	v_cvt_pk_bf16_f32 v57, v52, v53
	v_pk_mul_f32 v[52:53], v[58:59], v[52:53] op_sel_hi:[0,1]
	s_lshl_b64 s[78:79], s[78:79], 11
	s_ashr_i32 s81, s80, 31
	v_cvt_pk_bf16_f32 v60, v52, v53
	v_lshl_add_u64 v[52:53], v[44:45], 0, s[78:79]
	s_lshl_b64 s[78:79], s[80:81], 11
	ds_write_b16 v92, v63 offset:5184
	ds_write_b16_d16_hi v92, v63 offset:5456
	ds_write_b16 v92, v62 offset:40000
	ds_write_b16_d16_hi v92, v62 offset:40272
	global_store_short v[52:53], v60, off
	v_lshl_add_u64 v[52:53], v[44:45], 0, s[78:79]
	global_store_short_d16_hi v[52:53], v60, off
	v_rcp_f32_e32 v52, v54
	v_rcp_f32_e32 v53, v55
	s_add_i32 s80, s76, s72
	s_sub_i32 s81, 0x1fff, s80
	s_and_b64 s[78:79], s[10:11], exec
	v_pk_mul_f32 v[38:39], v[38:39], v[52:53]
	s_cselect_b32 s78, s80, s81
	v_cvt_pk_bf16_f32 v52, v38, v39
	v_pk_mul_f32 v[38:39], v[54:55], v[50:51]
	v_add_f32_e32 v50, v96, v139
	v_add_f32_e32 v51, v97, v139
	s_add_i32 s78, s78, s59
	v_max_f32_e32 v50, 0xc2e60000, v50
	v_max_f32_e32 v51, 0xc2e60000, v51
	s_add_i32 s80, s78, s64
	s_ashr_i32 s79, s78, 31
	v_exp_f32_e32 v50, v50
	v_exp_f32_e32 v51, v51
	v_cvt_pk_bf16_f32 v53, v38, v39
	v_pk_mul_f32 v[38:39], v[58:59], v[38:39] op_sel_hi:[0,1]
	s_lshl_b64 s[78:79], s[78:79], 11
	s_ashr_i32 s81, s80, 31
	v_cvt_pk_bf16_f32 v54, v38, v39
	v_lshl_add_u64 v[38:39], v[44:45], 0, s[78:79]
	s_lshl_b64 s[78:79], s[80:81], 11
	ds_write_b16 v92, v57 offset:5728
	ds_write_b16_d16_hi v92, v57 offset:6000
	ds_write_b16 v92, v56 offset:40544
	ds_write_b16_d16_hi v92, v56 offset:40816
	global_store_short v[38:39], v54, off
	v_lshl_add_u64 v[38:39], v[44:45], 0, s[78:79]
	global_store_short_d16_hi v[38:39], v54, off
	v_rcp_f32_e32 v38, v50
	v_rcp_f32_e32 v39, v51
	s_add_i32 s80, s76, s73
	s_sub_i32 s81, 0x1fff, s80
	s_and_b64 s[78:79], s[10:11], exec
	v_pk_mul_f32 v[34:35], v[34:35], v[38:39]
	s_cselect_b32 s78, s80, s81
	v_add_f32_e32 v38, v94, v139
	v_add_f32_e32 v39, v95, v139
	s_add_i32 s78, s78, s59
	v_max_f32_e32 v38, 0xc2e60000, v38
	v_max_f32_e32 v39, 0xc2e60000, v39
	ds_write_b16 v92, v53 offset:6272
	ds_write_b16_d16_hi v92, v53 offset:6544
	ds_write_b16 v92, v52 offset:41088
	ds_write_b16_d16_hi v92, v52 offset:41360
	v_cvt_pk_bf16_f32 v52, v34, v35
	v_pk_mul_f32 v[34:35], v[50:51], v[48:49]
	s_add_i32 s80, s78, s64
	s_ashr_i32 s79, s78, 31
	v_exp_f32_e32 v38, v38
	v_exp_f32_e32 v39, v39
	v_cvt_pk_bf16_f32 v48, v34, v35
	v_pk_mul_f32 v[34:35], v[58:59], v[34:35] op_sel_hi:[0,1]
	s_lshl_b64 s[78:79], s[78:79], 11
	s_ashr_i32 s81, s80, 31
	v_cvt_pk_bf16_f32 v49, v34, v35
	v_lshl_add_u64 v[34:35], v[44:45], 0, s[78:79]
	s_lshl_b64 s[78:79], s[80:81], 11
	global_store_short v[34:35], v49, off
	v_lshl_add_u64 v[34:35], v[44:45], 0, s[78:79]
	global_store_short_d16_hi v[34:35], v49, off
	v_rcp_f32_e32 v34, v38
	v_rcp_f32_e32 v35, v39
	s_add_i32 s76, s76, s74
	s_sub_i32 s80, 0x1fff, s76
	s_and_b64 s[78:79], s[10:11], exec
	s_cselect_b32 s76, s76, s80
	v_pk_mul_f32 v[32:33], v[32:33], v[34:35]
	s_add_i32 s78, s76, s59
	v_cvt_pk_bf16_f32 v34, v32, v33
	v_pk_mul_f32 v[32:33], v[38:39], v[36:37]
	s_add_i32 s80, s78, s64
	s_ashr_i32 s79, s78, 31
	v_cvt_pk_bf16_f32 v35, v32, v33
	v_pk_mul_f32 v[32:33], v[58:59], v[32:33] op_sel_hi:[0,1]
	s_lshl_b64 s[78:79], s[78:79], 11
	s_ashr_i32 s81, s80, 31
	v_cvt_pk_bf16_f32 v36, v32, v33
	v_lshl_add_u64 v[32:33], v[44:45], 0, s[78:79]
	s_lshl_b64 s[78:79], s[80:81], 11
	s_add_i32 s76, s75, 1
	ds_write_b16 v92, v48 offset:6816
	ds_write_b16_d16_hi v92, v48 offset:7088
	ds_write_b16 v92, v52 offset:41632
	ds_write_b16_d16_hi v92, v52 offset:41904
	global_store_short v[32:33], v36, off
	v_lshl_add_u64 v[32:33], v[44:45], 0, s[78:79]
	s_lshl_b32 s78, s76, 6
	s_cmp_lg_u32 s75, 7
	s_cselect_b32 s75, s78, 0x1c0
	s_add_i32 s75, s75, s61
	s_sub_i32 s80, 0x1fff, s75
	s_and_b64 s[78:79], s[10:11], exec
	s_cselect_b32 s78, s75, s80
	s_add_i32 s78, s78, s59
	s_ashr_i32 s79, s78, 31
	s_lshl_b64 s[80:81], s[78:79], 11
	global_store_short_d16_hi v[32:33], v36, off
	v_lshl_add_u64 v[32:33], v[44:45], 0, s[80:81]
	s_lshl_b64 s[78:79], s[78:79], 10
	s_or_b32 s80, s75, 1
	s_sub_i32 s81, 0x1ffe, s75
	ds_write_b16 v92, v35 offset:7360
	ds_write_b16_d16_hi v92, v35 offset:7632
	ds_write_b16 v92, v34 offset:42176
	ds_write_b16_d16_hi v92, v34 offset:42448
	v_or_b32_e32 v34, s78, v81
	v_mov_b32_e32 v35, s79
	s_and_b64 s[78:79], s[10:11], exec
	s_cselect_b32 s78, s80, s81
	s_add_i32 s78, s78, s59
	s_ashr_i32 s79, s78, 31
	s_lshl_b64 s[80:81], s[78:79], 11
	v_lshl_add_u64 v[38:39], v[44:45], 0, s[80:81]
	s_lshl_b64 s[78:79], s[78:79], 10
	s_or_b32 s80, s75, 2
	s_sub_i32 s81, 0x1ffd, s75
	v_or_b32_e32 v48, s78, v81
	v_mov_b32_e32 v49, s79
	s_and_b64 s[78:79], s[10:11], exec
	s_cselect_b32 s78, s80, s81
	s_add_i32 s78, s78, s59
	s_ashr_i32 s79, s78, 31
	s_lshl_b64 s[80:81], s[78:79], 11
	v_lshl_add_u64 v[56:57], v[44:45], 0, s[80:81]
	s_lshl_b64 s[78:79], s[78:79], 10
	s_or_b32 s80, s75, 3
	s_sub_i32 s81, 0x1ffc, s75
	v_or_b32_e32 v60, s78, v81
	v_mov_b32_e32 v61, s79
	s_and_b64 s[78:79], s[10:11], exec
	s_cselect_b32 s78, s80, s81
	s_add_i32 s78, s78, s59
	s_ashr_i32 s79, s78, 31
	v_lshl_add_u64 v[36:37], s[30:31], 0, v[34:35]
	v_lshl_add_u64 v[34:35], s[34:35], 0, v[34:35]
	v_lshl_add_u64 v[54:55], s[30:31], 0, v[48:49]
	s_lshl_b64 s[80:81], s[78:79], 11
	s_waitcnt lgkmcnt(0)
	s_barrier
	v_lshl_add_u64 v[48:49], s[34:35], 0, v[48:49]
	v_lshl_add_u64 v[62:63], s[30:31], 0, v[60:61]
	global_load_ushort v160, v[32:33], off
	global_load_ushort v50, v[36:37], off
	global_load_ushort v52, v[34:35], off
	global_load_ushort v161, v[38:39], off
	global_load_ushort v51, v[54:55], off
	global_load_ushort v53, v[48:49], off
	global_load_ushort v164, v[56:57], off
	s_nop 0
	global_load_ushort v54, v[62:63], off
	v_lshl_add_u64 v[34:35], v[44:45], 0, s[80:81]
	s_lshl_b64 s[78:79], s[78:79], 10
	s_or_b32 s80, s75, 4
	s_sub_i32 s81, 0x1ffb, s75
	v_or_b32_e32 v36, s78, v81
	v_mov_b32_e32 v37, s79
	s_and_b64 s[78:79], s[10:11], exec
	s_cselect_b32 s78, s80, s81
	s_add_i32 s78, s78, s59
	s_ashr_i32 s79, s78, 31
	s_lshl_b64 s[80:81], s[78:79], 11
	v_lshl_add_u64 v[32:33], s[34:35], 0, v[60:61]
	v_lshl_add_u64 v[60:61], v[44:45], 0, s[80:81]
	s_lshl_b64 s[78:79], s[78:79], 10
	s_or_b32 s80, s75, 5
	s_sub_i32 s81, 0x1ffa, s75
	v_or_b32_e32 v48, s78, v81
	v_mov_b32_e32 v49, s79
	s_and_b64 s[78:79], s[10:11], exec
	s_cselect_b32 s78, s80, s81
	s_add_i32 s78, s78, s59
	s_ashr_i32 s79, s78, 31
	s_lshl_b64 s[80:81], s[78:79], 11
	v_lshl_add_u64 v[86:87], v[44:45], 0, s[80:81]
	s_lshl_b64 s[78:79], s[78:79], 10
	s_or_b32 s80, s75, 6
	s_sub_i32 s81, 0x1ff9, s75
	v_lshl_add_u64 v[38:39], s[30:31], 0, v[36:37]
	v_lshl_add_u64 v[36:37], s[34:35], 0, v[36:37]
	v_lshl_add_u64 v[62:63], s[30:31], 0, v[48:49]
	v_lshl_add_u64 v[64:65], s[34:35], 0, v[48:49]
	global_load_ushort v56, v[32:33], off
	global_load_ushort v165, v[34:35], off
	global_load_ushort v48, v[38:39], off
	global_load_ushort v57, v[36:37], off
	global_load_ushort v166, v[60:61], off
	global_load_ushort v49, v[62:63], off
	global_load_ushort v58, v[64:65], off
	global_load_ushort v167, v[86:87], off
	v_or_b32_e32 v32, s78, v81
	v_mov_b32_e32 v33, s79
	s_and_b64 s[78:79], s[10:11], exec
	s_cselect_b32 s78, s80, s81
	s_add_i32 s78, s78, s59
	s_ashr_i32 s79, s78, 31
	s_lshl_b64 s[80:81], s[78:79], 11
	v_lshl_add_u64 v[36:37], v[44:45], 0, s[80:81]
	s_lshl_b64 s[78:79], s[78:79], 10
	s_or_b32 s80, s75, 7
	s_sub_i32 s81, 0x1ff8, s75
	v_or_b32_e32 v38, s78, v81
	v_mov_b32_e32 v39, s79
	s_and_b64 s[78:79], s[10:11], exec
	s_cselect_b32 s78, s80, s81
	s_add_i32 s78, s78, s59
	s_ashr_i32 s79, s78, 31
	s_lshl_b64 s[80:81], s[78:79], 11
	v_lshl_add_u64 v[64:65], v[44:45], 0, s[80:81]
	s_lshl_b64 s[78:79], s[78:79], 10
	s_or_b32 s80, s75, 8
	s_sub_i32 s81, 0x1ff7, s75
	v_or_b32_e32 v62, s78, v81
	v_mov_b32_e32 v63, s79
	s_and_b64 s[78:79], s[10:11], exec
	s_cselect_b32 s78, s80, s81
	s_add_i32 s78, s78, s59
	s_ashr_i32 s79, s78, 31
	v_lshl_add_u64 v[34:35], s[30:31], 0, v[32:33]
	v_lshl_add_u64 v[32:33], s[34:35], 0, v[32:33]
	v_lshl_add_u64 v[60:61], s[30:31], 0, v[38:39]
	s_lshl_b64 s[80:81], s[78:79], 11
	v_lshl_add_u64 v[38:39], s[34:35], 0, v[38:39]
	v_lshl_add_u64 v[86:87], s[30:31], 0, v[62:63]
	v_lshl_add_u64 v[88:89], s[34:35], 0, v[62:63]
	global_load_ushort v55, v[34:35], off
	global_load_ushort v62, v[32:33], off
	global_load_ushort v162, v[36:37], off
	s_nop 0
	global_load_ushort v60, v[60:61], off
	s_nop 0
	global_load_ushort v63, v[38:39], off
	global_load_ushort v163, v[64:65], off
	global_load_ushort v61, v[86:87], off
	s_nop 0
	global_load_ushort v64, v[88:89], off
	v_lshl_add_u64 v[32:33], v[44:45], 0, s[80:81]
	s_lshl_b64 s[78:79], s[78:79], 10
	s_or_b32 s80, s75, 9
	s_sub_i32 s81, 0x1ff6, s75
	v_or_b32_e32 v34, s78, v81
	v_mov_b32_e32 v35, s79
	s_and_b64 s[78:79], s[10:11], exec
	s_cselect_b32 s78, s80, s81
	s_add_i32 s78, s78, s59
	s_ashr_i32 s79, s78, 31
	s_lshl_b64 s[80:81], s[78:79], 11
	v_lshl_add_u64 v[38:39], v[44:45], 0, s[80:81]
	s_lshl_b64 s[78:79], s[78:79], 10
	s_or_b32 s80, s75, 10
	s_sub_i32 s81, 0x1ff5, s75
	v_or_b32_e32 v86, s78, v81
	v_mov_b32_e32 v87, s79
	s_and_b64 s[78:79], s[10:11], exec
	s_cselect_b32 s78, s80, s81
	s_add_i32 s78, s78, s59
	s_ashr_i32 s79, s78, 31
	s_lshl_b64 s[80:81], s[78:79], 11
	v_lshl_add_u64 v[92:93], v[44:45], 0, s[80:81]
	s_lshl_b64 s[78:79], s[78:79], 10
	s_or_b32 s80, s75, 11
	s_sub_i32 s81, 0x1ff4, s75
	v_or_b32_e32 v106, s78, v81
	v_mov_b32_e32 v107, s79
	s_and_b64 s[78:79], s[10:11], exec
	s_cselect_b32 s78, s80, s81
	s_add_i32 s78, s78, s59
	s_ashr_i32 s79, s78, 31
	v_lshl_add_u64 v[36:37], s[30:31], 0, v[34:35]
	v_lshl_add_u64 v[34:35], s[34:35], 0, v[34:35]
	v_lshl_add_u64 v[90:91], s[30:31], 0, v[86:87]
	s_lshl_b64 s[80:81], s[78:79], 11
	v_lshl_add_u64 v[86:87], s[34:35], 0, v[86:87]
	v_lshl_add_u64 v[108:109], s[30:31], 0, v[106:107]
	global_load_ushort v169, v[32:33], off
	global_load_ushort v88, v[36:37], off
	global_load_ushort v65, v[34:35], off
	global_load_ushort v168, v[38:39], off
	global_load_ushort v89, v[90:91], off
	global_load_ushort v100, v[86:87], off
	global_load_ushort v170, v[92:93], off
	s_nop 0
	global_load_ushort v90, v[108:109], off
	v_lshl_add_u64 v[34:35], v[44:45], 0, s[80:81]
	s_lshl_b64 s[78:79], s[78:79], 10
	s_or_b32 s80, s75, 12
	s_sub_i32 s81, 0x1ff3, s75
	v_or_b32_e32 v36, s78, v81
	v_mov_b32_e32 v37, s79
	s_and_b64 s[78:79], s[10:11], exec
	s_cselect_b32 s78, s80, s81
	s_add_i32 s78, s78, s59
	s_ashr_i32 s79, s78, 31
	s_lshl_b64 s[80:81], s[78:79], 11
	v_lshl_add_u64 v[92:93], v[44:45], 0, s[80:81]
	s_lshl_b64 s[78:79], s[78:79], 10
	s_or_b32 s80, s75, 13
	s_sub_i32 s81, 0x1ff2, s75
	v_or_b32_e32 v86, s78, v81
	v_mov_b32_e32 v87, s79
	s_and_b64 s[78:79], s[10:11], exec
	s_cselect_b32 s78, s80, s81
	s_add_i32 s78, s78, s59
	s_ashr_i32 s79, s78, 31
	s_lshl_b64 s[80:81], s[78:79], 11
	v_lshl_add_u64 v[32:33], s[34:35], 0, v[106:107]
	v_lshl_add_u64 v[112:113], s[34:35], 0, v[86:87]
	v_lshl_add_u64 v[116:117], v[44:45], 0, s[80:81]
	s_lshl_b64 s[78:79], s[78:79], 10
	s_or_b32 s80, s75, 14
	s_sub_i32 s81, 0x1ff1, s75
	v_lshl_add_u64 v[38:39], s[30:31], 0, v[36:37]
	v_lshl_add_u64 v[36:37], s[34:35], 0, v[36:37]
	v_lshl_add_u64 v[108:109], s[30:31], 0, v[86:87]
	global_load_ushort v105, v[32:33], off
	global_load_ushort v175, v[34:35], off
	global_load_ushort v86, v[38:39], off
	global_load_ushort v106, v[36:37], off
	global_load_ushort v171, v[92:93], off
	global_load_ushort v87, v[108:109], off
	global_load_ushort v107, v[112:113], off
	s_nop 0
	global_load_ushort v174, v[116:117], off
	v_or_b32_e32 v32, s78, v81
	v_mov_b32_e32 v33, s79
	s_and_b64 s[78:79], s[10:11], exec
	s_cselect_b32 s78, s80, s81
	s_add_i32 s78, s78, s59
	s_ashr_i32 s79, s78, 31
	s_lshl_b64 s[80:81], s[78:79], 11
	v_lshl_add_u64 v[36:37], v[44:45], 0, s[80:81]
	s_lshl_b64 s[78:79], s[78:79], 10
	s_or_b32 s80, s75, 15
	s_sub_i32 s75, 0x1ff0, s75
	v_or_b32_e32 v38, s78, v81
	v_mov_b32_e32 v39, s79
	s_and_b64 s[78:79], s[10:11], exec
	s_cselect_b32 s75, s80, s75
	s_add_i32 s78, s75, s59
	s_ashr_i32 s79, s78, 31
	s_lshl_b64 s[80:81], s[78:79], 11
	s_lshl_b64 s[78:79], s[78:79], 10
	v_lshl_add_u64 v[34:35], s[30:31], 0, v[32:33]
	v_lshl_add_u64 v[92:93], s[30:31], 0, v[38:39]
	v_lshl_add_u64 v[116:117], v[44:45], 0, s[80:81]
	v_or_b32_e32 v108, s78, v81
	v_mov_b32_e32 v109, s79
	v_lshl_add_u64 v[32:33], s[34:35], 0, v[32:33]
	v_lshl_add_u64 v[38:39], s[34:35], 0, v[38:39]
	v_lshl_add_u64 v[118:119], s[30:31], 0, v[108:109]
	v_lshl_add_u64 v[120:121], s[34:35], 0, v[108:109]
	global_load_ushort v91, v[34:35], off
	global_load_ushort v112, v[32:33], off
	global_load_ushort v172, v[36:37], off
	s_nop 0
	global_load_ushort v92, v[92:93], off
	s_nop 0
	global_load_ushort v108, v[38:39], off
	s_nop 0
	global_load_ushort v173, v[116:117], off
	s_nop 0
	global_load_ushort v93, v[118:119], off
	global_load_ushort v109, v[120:121], off
	ds_read_b128 v[36:39], v82
	ds_read_b128 v[32:35], v82 offset:64
	s_andn2_b64 vcc, exec, s[38:39]
	v_mov_b32_e32 v117, v78
	v_mov_b32_e32 v118, v77
	s_mov_b32 s75, s57
	s_cbranch_vccnz .LBB0_357

.LBB0_357:
	v_add_u32_e32 v117, 0x1000, v83
	ds_read2_b64 v[118:121], v117 offset1:4
	v_add_u32_e32 v152, 0x2000, v83
	v_add_u32_e32 v156, 0x3000, v83
	v_add_u32_e32 v157, 0x4000, v83
	ds_read2_b64 v[122:125], v152 offset0:32 offset1:36
	ds_read2_b64 v[132:135], v156 offset0:64 offset1:68
	ds_read2_b64 v[136:139], v157 offset0:96 offset1:100
	ds_read2_b64 v[140:143], v117 offset0:8 offset1:12
	v_cvt_pk_bf16_f32 v126, v0, v1
	v_cvt_pk_bf16_f32 v127, v2, v3
	v_cvt_pk_bf16_f32 v128, v4, v5
	v_cvt_pk_bf16_f32 v129, v6, v7
	ds_read2_b64 v[144:147], v152 offset0:40 offset1:44
	v_cvt_pk_bf16_f32 v148, v16, v17
	s_waitcnt lgkmcnt(5)
	v_mfma_f32_16x16x32_bf16 v[118:121], v[118:121], v[126:129], 0
	v_cvt_pk_bf16_f32 v149, v18, v19
	v_cvt_pk_bf16_f32 v150, v20, v21
	v_cvt_pk_bf16_f32 v151, v22, v23
	s_waitcnt lgkmcnt(4)
	v_mfma_f32_16x16x32_bf16 v[122:125], v[122:125], v[126:129], 0
	v_add_f32_e32 v69, v69, v59
	s_nop 0
	s_nop 0
	s_nop 0
	s_nop 0
	s_waitcnt lgkmcnt(3)
	v_mfma_f32_16x16x32_bf16 v[132:135], v[132:135], v[126:129], 0
	s_nop 0
	s_nop 0
	s_nop 0
	s_nop 0
	s_nop 0
	s_nop 0
	s_waitcnt lgkmcnt(2)
	v_mfma_f32_16x16x32_bf16 v[126:129], v[136:139], v[126:129], 0
	v_cvt_pk_bf16_f32 v136, v8, v9
	v_cvt_pk_bf16_f32 v137, v10, v11
	v_cvt_pk_bf16_f32 v138, v12, v13
	v_cvt_pk_bf16_f32 v139, v14, v15
	s_cmp_eq_u32 s76, 8
	s_nop 0
	s_nop 0
	s_waitcnt lgkmcnt(1)
	v_mfma_f32_16x16x32_bf16 v[118:121], v[140:143], v[136:139], v[118:121]
	ds_read2_b64 v[140:143], v156 offset0:72 offset1:76
	s_waitcnt lgkmcnt(1)
	v_mfma_f32_16x16x32_bf16 v[122:125], v[144:147], v[136:139], v[122:125]
	ds_read2_b64 v[144:147], v157 offset0:104 offset1:108
	s_waitcnt lgkmcnt(1)
	v_mfma_f32_16x16x32_bf16 v[132:135], v[140:143], v[136:139], v[132:135]
	ds_read2_b64 v[140:143], v117 offset0:16 offset1:20
	s_waitcnt lgkmcnt(1)
	v_mfma_f32_16x16x32_bf16 v[126:129], v[144:147], v[136:139], v[126:129]
	ds_read2_b64 v[136:139], v152 offset0:48 offset1:52
	ds_read2_b64 v[144:147], v157 offset0:112 offset1:116
	ds_read2_b64 v[152:155], v152 offset0:56 offset1:60
	s_waitcnt lgkmcnt(3)
	v_mfma_f32_16x16x32_bf16 v[118:121], v[140:143], v[148:151], v[118:121]
	ds_read2_b64 v[140:143], v156 offset0:80 offset1:84
	s_waitcnt lgkmcnt(3)
	v_mfma_f32_16x16x32_bf16 v[122:125], v[136:139], v[148:151], v[122:125]
	ds_read2_b64 v[136:139], v117 offset0:24 offset1:28
	s_waitcnt lgkmcnt(3)
	v_mfma_f32_16x16x32_bf16 v[126:129], v[144:147], v[148:151], v[126:129]
	ds_read2_b64 v[144:147], v156 offset0:88 offset1:92
	s_nop 0
	s_waitcnt lgkmcnt(2)
	v_mfma_f32_16x16x32_bf16 v[132:135], v[140:143], v[148:151], v[132:135]
	v_cvt_pk_bf16_f32 v140, v24, v25
	v_cvt_pk_bf16_f32 v141, v26, v27
	v_cvt_pk_bf16_f32 v142, v28, v29
	v_cvt_pk_bf16_f32 v143, v30, v31
	s_waitcnt lgkmcnt(1)
	s_nop 0
	v_mfma_f32_16x16x32_bf16 v[118:121], v[136:139], v[140:143], v[118:121]
	ds_read2_b64 v[136:139], v157 offset0:120 offset1:124
	s_waitcnt lgkmcnt(0)
	s_barrier
	ds_read_b128 v[148:151], v84
	v_mfma_f32_16x16x32_bf16 v[132:135], v[144:147], v[140:143], v[132:135]
	ds_read_b128 v[144:147], v84 offset:2304
	v_mfma_f32_16x16x32_bf16 v[122:125], v[152:155], v[140:143], v[122:125]
	s_nop 0
	s_nop 0
	s_nop 0
	s_waitcnt lgkmcnt(0)
	v_mfma_f32_16x16x32_bf16 v[122:125], v[144:147], v[36:39], v[122:125]
	s_nop 0
	v_add_u32_e32 v103, s77, v75
	v_sub_u32_e32 v98, 0x1fff, v103
	v_mfma_f32_16x16x32_bf16 v[118:121], v[148:151], v[36:39], v[118:121]
	s_nop 0
	v_cndmask_b32_e64 v104, v98, v103, s[10:11]
	v_add_u32_e32 v98, s59, v104
	v_ashrrev_i32_e32 v99, 31, v98
	v_lshlrev_b64 v[98:99], 10, v[98:99]
	s_nop 0
	s_nop 1
	v_cvt_pk_bf16_f32 v110, v118, v119
	v_lshl_add_u64 v[98:99], v[46:47], 0, v[98:99]
	global_store_short v[98:99], v110, off
	v_add_u32_e32 v98, s65, v104
	v_ashrrev_i32_e32 v99, 31, v98
	v_lshlrev_b64 v[98:99], 10, v[98:99]
	v_lshl_add_u64 v[98:99], v[46:47], 0, v[98:99]
	global_store_short_d16_hi v[98:99], v110, off
	v_or_b32_e32 v98, 2, v103
	v_sub_u32_e32 v99, 0x1ffd, v103
	v_cndmask_b32_e64 v104, v99, v98, s[10:11]
	v_add_u32_e32 v98, s59, v104
	v_ashrrev_i32_e32 v99, 31, v98
	v_lshlrev_b64 v[98:99], 10, v[98:99]
	v_cvt_pk_bf16_f32 v110, v120, v121
	v_lshl_add_u64 v[98:99], v[46:47], 0, v[98:99]
	global_store_short v[98:99], v110, off
	v_add_u32_e32 v98, s65, v104
	v_ashrrev_i32_e32 v99, 31, v98
	v_lshlrev_b64 v[98:99], 10, v[98:99]
	v_lshl_add_u64 v[98:99], v[46:47], 0, v[98:99]
	global_store_short_d16_hi v[98:99], v110, off
	v_or_b32_e32 v98, 16, v103
	v_sub_u32_e32 v99, 0x1fef, v103
	v_cndmask_b32_e64 v104, v99, v98, s[10:11]
	v_add_u32_e32 v98, s59, v104
	v_ashrrev_i32_e32 v99, 31, v98
	v_lshlrev_b64 v[98:99], 10, v[98:99]
	ds_read_b128 v[94:97], v84 offset:4608
	v_cvt_pk_bf16_f32 v110, v122, v123
	v_lshl_add_u64 v[98:99], v[46:47], 0, v[98:99]
	global_store_short v[98:99], v110, off
	v_add_u32_e32 v98, s65, v104
	v_ashrrev_i32_e32 v99, 31, v98
	v_lshlrev_b64 v[98:99], 10, v[98:99]
	v_mfma_f32_16x16x32_bf16 v[126:129], v[136:139], v[140:143], v[126:129]
	ds_read_b128 v[136:139], v84 offset:4672
	v_lshl_add_u64 v[98:99], v[46:47], 0, v[98:99]
	global_store_short_d16_hi v[98:99], v110, off
	v_or_b32_e32 v98, 18, v103
	v_sub_u32_e32 v99, 0x1fed, v103
	v_cndmask_b32_e64 v104, v99, v98, s[10:11]
	v_add_u32_e32 v98, s59, v104
	v_ashrrev_i32_e32 v99, 31, v98
	s_waitcnt lgkmcnt(1)
	v_mfma_f32_16x16x32_bf16 v[94:97], v[94:97], v[36:39], v[132:135]
	v_lshlrev_b64 v[98:99], 10, v[98:99]
	v_cvt_pk_bf16_f32 v110, v124, v125
	v_lshl_add_u64 v[98:99], v[46:47], 0, v[98:99]
	global_store_short v[98:99], v110, off
	v_add_u32_e32 v98, s65, v104
	v_ashrrev_i32_e32 v99, 31, v98
	s_waitcnt lgkmcnt(0)
	v_mfma_f32_16x16x32_bf16 v[94:97], v[136:139], v[32:35], v[94:97]
	v_lshlrev_b64 v[98:99], 10, v[98:99]
	v_lshl_add_u64 v[98:99], v[46:47], 0, v[98:99]
	global_store_short_d16_hi v[98:99], v110, off
	v_or_b32_e32 v98, 32, v103
	v_sub_u32_e32 v99, 0x1fdf, v103
	v_cndmask_b32_e64 v98, v99, v98, s[10:11]
	s_nop 1
	v_cvt_pk_bf16_f32 v99, v94, v95
	v_add_u32_e32 v94, s59, v98
	v_ashrrev_i32_e32 v95, 31, v94
	v_lshlrev_b64 v[94:95], 10, v[94:95]
	v_lshl_add_u64 v[94:95], v[46:47], 0, v[94:95]
	global_store_short v[94:95], v99, off
	v_add_u32_e32 v94, s65, v98
	v_ashrrev_i32_e32 v95, 31, v94
	ds_read_b128 v[140:143], v84 offset:6912
	ds_read_b128 v[132:135], v84 offset:6976
	v_lshlrev_b64 v[94:95], 10, v[94:95]
	v_lshl_add_u64 v[94:95], v[46:47], 0, v[94:95]
	global_store_short_d16_hi v[94:95], v99, off
	v_or_b32_e32 v94, 34, v103
	v_sub_u32_e32 v95, 0x1fdd, v103
	v_cndmask_b32_e64 v98, v95, v94, s[10:11]
	v_add_u32_e32 v94, s59, v98
	v_ashrrev_i32_e32 v95, 31, v94
	v_lshlrev_b64 v[94:95], 10, v[94:95]
	v_cvt_pk_bf16_f32 v96, v96, v97
	v_lshl_add_u64 v[94:95], v[46:47], 0, v[94:95]
	global_store_short v[94:95], v96, off
	v_add_u32_e32 v94, s65, v98
	s_nop 0
	s_nop 0
	s_nop 0
	s_waitcnt lgkmcnt(1)
	v_mfma_f32_16x16x32_bf16 v[114:117], v[140:143], v[36:39], v[126:129]
	v_ashrrev_i32_e32 v95, 31, v94
	v_lshlrev_b64 v[94:95], 10, v[94:95]
	v_lshl_add_u64 v[94:95], v[46:47], 0, v[94:95]
	global_store_short_d16_hi v[94:95], v96, off
	v_or_b32_e32 v94, 48, v103
	v_sub_u32_e32 v95, 0x1fcf, v103
	s_waitcnt lgkmcnt(0)
	v_mfma_f32_16x16x32_bf16 v[114:117], v[132:135], v[32:35], v[114:117]
	v_cndmask_b32_e64 v96, v95, v94, s[10:11]
	v_add_u32_e32 v94, s59, v96
	v_ashrrev_i32_e32 v95, 31, v94
	v_lshlrev_b64 v[94:95], 10, v[94:95]
	v_lshl_add_u64 v[94:95], v[46:47], 0, v[94:95]
	s_nop 2
	v_cvt_pk_bf16_f32 v97, v114, v115
	global_store_short v[94:95], v97, off
	v_add_u32_e32 v94, s65, v96
	v_ashrrev_i32_e32 v95, 31, v94
	v_lshlrev_b64 v[94:95], 10, v[94:95]
	v_lshl_add_u64 v[94:95], v[46:47], 0, v[94:95]
	global_store_short_d16_hi v[94:95], v97, off
	v_add_u32_e32 v104, v74, v73
	ds_read_b128 v[94:97], v85
	ds_read_b128 v[118:121], v104 offset:2048
	ds_read_b128 v[122:125], v85 offset:64
	ds_read_b128 v[126:129], v104 offset:2112
	v_cvt_pk_bf16_f32 v110, v116, v117
	v_or_b32_e32 v98, 50, v103
	v_sub_u32_e32 v99, 0x1fcd, v103
	s_waitcnt lgkmcnt(2)
	v_pk_mul_f32 v[0:1], v[0:1], v[118:119]
	v_pk_mul_f32 v[2:3], v[2:3], v[120:121]
	ds_read_b128 v[118:121], v85 offset:2304
	s_waitcnt lgkmcnt(1)
	v_pk_mul_f32 v[4:5], v[4:5], v[126:127]
	v_mfma_f32_16x16x32_bf16 v[0:3], v[94:97], v[36:39], v[0:3]
	ds_read_b128 v[94:97], v85 offset:2368
	v_pk_mul_f32 v[6:7], v[6:7], v[128:129]
	v_cndmask_b32_e64 v103, v99, v98, s[10:11]
	v_mfma_f32_16x16x32_bf16 v[0:3], v[122:125], v[32:35], v[0:3]
	ds_read_b128 v[122:125], v104 offset:2176
	ds_read_b128 v[126:129], v85 offset:4608
	v_add_u32_e32 v98, s59, v103
	v_ashrrev_i32_e32 v99, 31, v98
	s_waitcnt lgkmcnt(3)
	v_mfma_f32_16x16x32_bf16 v[4:7], v[118:121], v[36:39], v[4:7]
	ds_read_b128 v[114:117], v104 offset:2240
	ds_read_b128 v[118:121], v85 offset:4672
	s_waitcnt lgkmcnt(3)
	v_pk_mul_f32 v[8:9], v[8:9], v[122:123]
	v_pk_mul_f32 v[10:11], v[10:11], v[124:125]
	v_mfma_f32_16x16x32_bf16 v[4:7], v[94:97], v[32:35], v[4:7]
	ds_read_b128 v[94:97], v85 offset:6912
	ds_read_b128 v[122:125], v85 offset:6976
	s_waitcnt lgkmcnt(3)
	v_pk_mul_f32 v[12:13], v[12:13], v[114:115]
	v_mfma_f32_16x16x32_bf16 v[8:11], v[126:129], v[36:39], v[8:11]
	v_mul_f32_e64 v14, v14, v116
	v_mul_f32_e64 v15, v15, v117
	v_lshlrev_b64 v[98:99], 10, v[98:99]
	v_lshl_add_u64 v[98:99], v[46:47], 0, v[98:99]
	s_waitcnt lgkmcnt(2)
	v_mfma_f32_16x16x32_bf16 v[8:11], v[118:121], v[32:35], v[8:11]
	ds_read_b128 v[114:117], v104 offset:2304
	ds_read_b128 v[118:121], v85 offset:9216
	s_nop 0
	s_nop 0
	s_waitcnt lgkmcnt(3)
	v_mfma_f32_16x16x32_bf16 v[12:15], v[94:97], v[36:39], v[12:15]
	ds_read_b128 v[94:97], v104 offset:2368
	ds_read_b128 v[126:129], v85 offset:9280
	s_waitcnt lgkmcnt(3)
	v_pk_mul_f32 v[16:17], v[16:17], v[114:115]
	v_pk_mul_f32 v[18:19], v[18:19], v[116:117]
	ds_read_b128 v[114:117], v85 offset:11520
	v_mfma_f32_16x16x32_bf16 v[12:15], v[122:125], v[32:35], v[12:15]
	s_waitcnt lgkmcnt(2)
	v_pk_mul_f32 v[20:21], v[20:21], v[94:95]
	v_pk_mul_f32 v[22:23], v[22:23], v[96:97]
	v_mfma_f32_16x16x32_bf16 v[16:19], v[118:121], v[36:39], v[16:19]
	ds_read_b128 v[118:121], v85 offset:11584
	ds_read_b128 v[94:97], v104 offset:2432
	ds_read_b128 v[122:125], v85 offset:13824
	s_waitcnt lgkmcnt(1)
	v_pk_mul_f32 v[24:25], v[24:25], v[94:95]
	v_mfma_f32_16x16x32_bf16 v[16:19], v[126:129], v[32:35], v[16:19]
	v_mul_f32_e64 v26, v26, v96
	v_mul_f32_e64 v27, v27, v97
	v_mfma_f32_16x16x32_bf16 v[20:23], v[114:117], v[36:39], v[20:23]
	ds_read_b128 v[114:117], v104 offset:2496
	ds_read_b128 v[126:129], v85 offset:13888
	ds_read_b128 v[94:97], v85 offset:16128
	global_store_short v[98:99], v110, off
	v_mfma_f32_16x16x32_bf16 v[20:23], v[118:121], v[32:35], v[20:23]
	v_add_u32_e32 v98, s65, v103
	ds_read_b128 v[118:121], v85 offset:16192
	s_waitcnt lgkmcnt(3)
	v_pk_mul_f32 v[28:29], v[28:29], v[114:115]
	s_waitcnt vmcnt(8)
	v_cvt_f32_f16_e32 v59, v160
	v_cvt_f32_f16_e32 v158, v161
	v_cvt_f32_f16_e32 v102, v162
	v_cvt_f32_f16_e32 v101, v163
	v_cvt_f32_f16_e32 v156, v164
	v_cvt_f32_f16_e32 v152, v165
	v_cvt_f32_f16_e32 v153, v166
	v_cvt_f32_f16_e32 v154, v167
	v_cvt_f32_f16_e32 v144, v168
	v_cvt_f32_f16_e32 v148, v169
	v_cvt_f32_f16_e32 v145, v170
	v_cvt_f32_f16_e32 v147, v171
	v_cvt_f32_f16_e32 v137, v172
	v_cvt_f32_f16_e32 v138, v173
	v_cvt_f32_f16_e32 v136, v174
	v_cvt_f32_f16_e32 v146, v175
	v_perm_b32 v105, v106, v105, s48
	v_perm_b32 v106, v109, v108, s48
	v_add_f32_e32 v115, 0, v59
	v_ashrrev_i32_e32 v99, 31, v98
	v_pk_mul_f32 v[30:31], v[30:31], v[116:117]
	v_add_f32_e32 v116, v115, v158
	v_mfma_f32_16x16x32_bf16 v[24:27], v[122:125], v[36:39], v[24:27]
	v_add_f32_e32 v113, v116, v156
	v_add_f32_e32 v114, v113, v152
	v_exp_f32_e32 v122, v101
	s_waitcnt lgkmcnt(1)
	v_mfma_f32_16x16x32_bf16 v[28:31], v[94:97], v[36:39], v[28:31]
	v_lshlrev_b64 v[36:37], 10, v[98:99]
	v_lshl_add_u64 v[36:37], v[46:47], 0, v[36:37]
	global_store_short_d16_hi v[36:37], v110, off
	v_add_f32_e32 v110, v114, v153
	v_add_f32_e32 v111, v110, v154
	v_add_f32_e32 v103, v111, v102
	v_add_f32_e32 v104, v103, v101
	v_add_f32_e32 v101, v104, v148
	s_waitcnt lgkmcnt(0)
	v_mfma_f32_16x16x32_bf16 v[28:31], v[118:121], v[32:35], v[28:31]
	v_exp_f32_e32 v121, v102
	v_add_f32_e32 v102, v101, v144
	v_add_f32_e32 v98, v102, v145
	v_add_f32_e32 v99, v98, v146
	v_mfma_f32_16x16x32_bf16 v[24:27], v[126:129], v[32:35], v[24:27]
	v_exp_f32_e32 v36, v59
	v_exp_f32_e32 v37, v158
	v_exp_f32_e32 v117, v156
	v_exp_f32_e32 v118, v152
	v_exp_f32_e32 v119, v153
	v_exp_f32_e32 v120, v154
	v_exp_f32_e32 v123, v148
	v_exp_f32_e32 v124, v144
	v_exp_f32_e32 v38, v145
	v_exp_f32_e32 v39, v146
	v_add_f32_e32 v96, v99, v147
	v_exp_f32_e32 v34, v147
	v_exp_f32_e32 v35, v136
	v_exp_f32_e32 v32, v137
	v_exp_f32_e32 v33, v138
	v_add_f32_e32 v97, v96, v136
	v_add_f32_e32 v94, v97, v137
	v_add_f32_e32 v95, v94, v138
	v_perm_b32 v129, v53, v52, s48
	v_perm_b32 v128, v57, v56, s48
	v_perm_b32 v127, v62, v58, s48
	v_perm_b32 v126, v64, v63, s48
	v_perm_b32 v125, v100, v65, s48
	v_perm_b32 v100, v112, v107, s48
	ds_write_b32 v70, v95
	s_waitcnt lgkmcnt(0)
	s_barrier
	s_cbranch_scc1 .LBB0_359
	s_mov_b32 s75, s76
	s_branch .LBB0_353
